# baseline (speedup 1.0000x reference)
.LBB1_8:
	s_or_b64 exec, exec, s[4:5]
	s_waitcnt vmcnt(1)
	v_mov_b32_e32 v184, 1
	v_lshl_add_u32 v180, v176, 2, v172
	v_lshl_add_u32 v181, v177, 2, v172
	v_lshl_add_u32 v182, v178, 2, v172
	v_lshl_add_u32 v183, v179, 2, v172
	ds_add_u32 v180, v184
	ds_add_u32 v181, v184
	ds_add_u32 v182, v184
	ds_add_u32 v183, v184
	s_waitcnt lgkmcnt(0)
	ds_read_b32 v151, v173
	s_waitcnt lgkmcnt(0)
	v_cvt_f32_i32_e32 v185, v151
	ds_write_b32 v173, v185 offset:256
	v_add_u32_e32 v10, v172, v2
	s_waitcnt vmcnt(1) lgkmcnt(0)
	s_barrier
	ds_read_b128 v[18:21], v10 offset:256
	ds_read_b128 v[22:25], v10 offset:288
	ds_read_b128 v[82:85], v10 offset:320
	ds_read_b128 v[86:89], v10 offset:352
	ds_read_b128 v[74:77], v10 offset:384
	ds_read_b128 v[78:81], v10 offset:416
	ds_read_b128 v[2:5], v213 offset:32768
	ds_read_b128 v[6:9], v213 offset:0
	ds_read_b128 v[66:69], v10 offset:448
	ds_read_b128 v[70:73], v10 offset:480
	ds_read_b128 v[10:13], v213 offset:1024
	s_waitcnt lgkmcnt(3)
	v_pk_mul_f32 v[26:27], v[8:9], v[20:21]
	v_pk_mul_f32 v[28:29], v[6:7], v[18:19]
	ds_read_b128 v[14:17], v213 offset:8192
	s_waitcnt lgkmcnt(1)
	v_pk_mul_f32 v[12:13], v[12:13], v[24:25]
	v_pk_mul_f32 v[10:11], v[10:11], v[22:23]
	v_pk_fma_f32 v[30:31], v[8:9], v[20:21], v[12:13]
	v_pk_fma_f32 v[32:33], v[6:7], v[18:19], v[10:11]
	v_cvt_pk_bf16_f32 v9, v12, v13
	v_cvt_pk_bf16_f32 v7, v26, v27
	v_cvt_pk_bf16_f32 v8, v10, v11
	v_cvt_pk_bf16_f32 v6, v28, v29
	ds_read_b128 v[10:13], v213 offset:33792
	s_nop 0
	v_mfma_f32_32x32x16_bf16 v[34:49], v[2:5], v[6:9], 0
	ds_read_b128 v[6:9], v213 offset:9216
	s_waitcnt lgkmcnt(2)
	v_mul_f32_e32 v26, v16, v20
	v_mul_f32_e32 v27, v17, v21
	v_pk_mul_f32 v[50:51], v[14:15], v[18:19]
	s_mov_b32 s4, 0x3727c5ac
	s_waitcnt lgkmcnt(0)
	v_pk_mul_f32 v[8:9], v[8:9], v[24:25]
	v_pk_mul_f32 v[28:29], v[6:7], v[22:23]
	v_pk_fma_f32 v[90:91], v[16:17], v[20:21], v[8:9]
	v_pk_fma_f32 v[92:93], v[14:15], v[18:19], v[28:29]
	ds_read_b128 v[14:17], v213 offset:2048
	v_cvt_pk_bf16_f32 v9, v8, v9
	v_cvt_pk_bf16_f32 v7, v26, v27
	v_cvt_pk_bf16_f32 v8, v28, v29
	ds_read_b128 v[26:29], v213 offset:3072
	v_cvt_pk_bf16_f32 v6, v50, v51
	s_waitcnt lgkmcnt(1)
	v_pk_mul_f32 v[94:95], v[14:15], v[82:83]
	s_mov_b32 s0, 0x3c800000
	v_mfma_f32_32x32x16_bf16 v[50:65], v[2:5], v[6:9], 0
	v_mul_f32_e32 v2, v16, v84
	v_mul_f32_e32 v3, v17, v85
	s_waitcnt lgkmcnt(0)
	v_mul_f32_e32 v4, v28, v88
	v_mul_f32_e32 v5, v29, v89
	v_pk_mul_f32 v[6:7], v[26:27], v[86:87]
	v_pk_fma_f32 v[8:9], v[16:17], v[84:85], v[4:5]
	v_cvt_pk_bf16_f32 v3, v2, v3
	v_pk_fma_f32 v[14:15], v[14:15], v[82:83], v[6:7]
	v_pk_add_f32 v[26:27], v[8:9], v[30:31]
	v_cvt_pk_bf16_f32 v5, v4, v5
	v_cvt_pk_bf16_f32 v4, v6, v7
	ds_read_b128 v[6:9], v213 offset:10240
	v_pk_add_f32 v[28:29], v[14:15], v[32:33]
	ds_read_b128 v[14:17], v213 offset:11264
	v_cvt_pk_bf16_f32 v2, v94, v95
	s_waitcnt lgkmcnt(1)
	v_pk_mul_f32 v[30:31], v[6:7], v[82:83]
	v_mov_b64_e32 v[152:153], s[4:5]
	v_mfma_f32_32x32x16_bf16 v[34:49], v[10:13], v[2:5], v[34:49]
	v_mul_f32_e32 v2, v8, v84
	v_mul_f32_e32 v3, v9, v85
	s_waitcnt lgkmcnt(0)
	v_mul_f32_e32 v4, v16, v88
	v_mul_f32_e32 v5, v17, v89
	v_pk_mul_f32 v[14:15], v[14:15], v[86:87]
	v_pk_fma_f32 v[8:9], v[8:9], v[84:85], v[4:5]
	v_pk_fma_f32 v[6:7], v[6:7], v[82:83], v[14:15]
	v_cvt_pk_bf16_f32 v5, v4, v5
	v_cvt_pk_bf16_f32 v3, v2, v3
	v_cvt_pk_bf16_f32 v4, v14, v15
	v_pk_add_f32 v[32:33], v[8:9], v[90:91]
	v_pk_add_f32 v[90:91], v[6:7], v[92:93]
	ds_read_b128 v[6:9], v213 offset:34816
	ds_read_b128 v[14:17], v213 offset:4096
	v_cvt_pk_bf16_f32 v2, v30, v31
	s_mov_b32 s13, 0
	s_mov_b64 s[6:7], 0
	v_mfma_f32_32x32x16_bf16 v[50:65], v[10:13], v[2:5], v[50:65]
	ds_read_b128 v[2:5], v213 offset:5120
	ds_read_b128 v[10:13], v213 offset:12288
	s_waitcnt lgkmcnt(2)
	v_pk_mul_f32 v[30:31], v[16:17], v[76:77]
	v_pk_mul_f32 v[92:93], v[14:15], v[74:75]
	s_waitcnt lgkmcnt(1)
	v_pk_mul_f32 v[4:5], v[4:5], v[80:81]
	v_pk_mul_f32 v[94:95], v[2:3], v[78:79]
	v_pk_fma_f32 v[2:3], v[16:17], v[76:77], v[4:5]
	v_cvt_pk_bf16_f32 v5, v4, v5
	v_pk_add_f32 v[96:97], v[2:3], v[26:27]
	v_cvt_pk_bf16_f32 v3, v30, v31
	v_cvt_pk_bf16_f32 v4, v94, v95
	v_cvt_pk_bf16_f32 v2, v92, v93
	v_pk_fma_f32 v[14:15], v[14:15], v[74:75], v[94:95]
	s_waitcnt lgkmcnt(0)
	v_pk_mul_f32 v[30:31], v[10:11], v[74:75]
	v_mfma_f32_32x32x16_bf16 v[34:49], v[6:9], v[2:5], v[34:49]
	ds_read_b128 v[2:5], v213 offset:13312
	v_add_f32_e32 v98, v14, v28
	v_add_f32_e32 v99, v15, v29
	ds_read_b128 v[14:17], v213 offset:35840
	v_pk_mul_f32 v[26:27], v[12:13], v[76:77]
	s_waitcnt lgkmcnt(1)
	v_pk_mul_f32 v[4:5], v[4:5], v[80:81]
	v_pk_mul_f32 v[28:29], v[2:3], v[78:79]
	v_pk_fma_f32 v[2:3], v[12:13], v[76:77], v[4:5]
	v_pk_fma_f32 v[10:11], v[10:11], v[74:75], v[28:29]
	v_pk_add_f32 v[32:33], v[2:3], v[32:33]
	v_pk_add_f32 v[92:93], v[10:11], v[90:91]
	ds_read_b128 v[10:13], v213 offset:6144
	v_cvt_pk_bf16_f32 v5, v4, v5
	v_cvt_pk_bf16_f32 v3, v26, v27
	v_cvt_pk_bf16_f32 v4, v28, v29
	ds_read_b128 v[26:29], v213 offset:7168
	v_cvt_pk_bf16_f32 v2, v30, v31
	s_waitcnt lgkmcnt(1)
	v_pk_mul_f32 v[30:31], v[10:11], v[66:67]
	v_mfma_f32_32x32x16_bf16 v[50:65], v[6:9], v[2:5], v[50:65]
	v_mul_f32_e32 v2, v12, v68
	v_mul_f32_e32 v3, v13, v69
	s_waitcnt lgkmcnt(0)
	v_mul_f32_e32 v4, v28, v72
	v_mul_f32_e32 v5, v29, v73
	v_pk_mul_f32 v[6:7], v[26:27], v[70:71]
	v_pk_fma_f32 v[8:9], v[12:13], v[68:69], v[4:5]
	v_cvt_pk_bf16_f32 v3, v2, v3
	v_pk_fma_f32 v[10:11], v[10:11], v[66:67], v[6:7]
	v_pk_add_f32 v[94:95], v[8:9], v[96:97]
	v_cvt_pk_bf16_f32 v5, v4, v5
	v_cvt_pk_bf16_f32 v4, v6, v7
	ds_read_b128 v[6:9], v213 offset:14336
	v_pk_add_f32 v[96:97], v[10:11], v[98:99]
	ds_read_b128 v[10:13], v213 offset:15360
	v_cvt_pk_bf16_f32 v2, v30, v31
	s_waitcnt lgkmcnt(1)
	v_pk_mul_f32 v[30:31], v[6:7], v[66:67]
	v_mfma_f32_32x32x16_bf16 v[34:49], v[14:17], v[2:5], v[34:49]
	s_waitcnt lgkmcnt(0)
	v_mul_f32_e32 v10, v10, v70
	v_mul_f32_e32 v11, v11, v71
	v_mul_f32_e32 v2, v8, v68
	v_mul_f32_e32 v3, v9, v69
	v_pk_mul_f32 v[4:5], v[12:13], v[72:73]
	v_pk_fma_f32 v[6:7], v[6:7], v[66:67], v[10:11]
	v_pk_fma_f32 v[8:9], v[8:9], v[68:69], v[4:5]
	v_pk_add_f32 v[92:93], v[6:7], v[92:93]
	v_cvt_pk_bf16_f32 v3, v2, v3
	v_pk_add_f32 v[90:91], v[8:9], v[32:33]
	v_cvt_pk_bf16_f32 v5, v4, v5
	v_cvt_pk_bf16_f32 v4, v10, v11
	ds_read_b128 v[26:29], v213 offset:36864
	ds_read_b128 v[6:9], v213 offset:16384
	v_cvt_pk_bf16_f32 v2, v30, v31
	ds_read_b128 v[98:101], v213 offset:25600
	ds_read_b128 v[102:105], v213 offset:37888
	v_mfma_f32_32x32x16_bf16 v[50:65], v[14:17], v[2:5], v[50:65]
	ds_read_b128 v[2:5], v213 offset:17408
	ds_read_b128 v[30:33], v213 offset:24576
	s_waitcnt lgkmcnt(4)
	v_pk_mul_f32 v[12:13], v[6:7], v[18:19]
	v_pk_mul_f32 v[10:11], v[8:9], v[20:21]
	s_waitcnt lgkmcnt(1)
	v_pk_mul_f32 v[14:15], v[2:3], v[22:23]
	v_pk_mul_f32 v[22:23], v[98:99], v[22:23]
	v_pk_fma_f32 v[112:113], v[6:7], v[18:19], v[14:15]
	s_waitcnt lgkmcnt(0)
	v_pk_mul_f32 v[114:115], v[30:31], v[18:19]
	v_pk_fma_f32 v[118:119], v[30:31], v[18:19], v[22:23]
	v_pk_mul_f32 v[4:5], v[4:5], v[24:25]
	v_pk_mul_f32 v[106:107], v[32:33], v[20:21]
	v_pk_mul_f32 v[24:25], v[100:101], v[24:25]
	ds_read_b128 v[98:101], v213 offset:18432
	v_cvt_pk_bf16_f32 v19, v106, v107
	ds_read_b128 v[106:109], v213 offset:19456
	v_pk_fma_f32 v[110:111], v[8:9], v[20:21], v[4:5]
	v_cvt_pk_bf16_f32 v5, v4, v5
	v_cvt_pk_bf16_f32 v3, v10, v11
	v_cvt_pk_bf16_f32 v4, v14, v15
	s_waitcnt lgkmcnt(0)
	v_pk_mul_f32 v[106:107], v[106:107], v[86:87]
	v_cvt_pk_bf16_f32 v2, v12, v13
	v_pk_mul_f32 v[120:121], v[98:99], v[82:83]
	v_pk_mul_f32 v[108:109], v[108:109], v[88:89]
	v_pk_fma_f32 v[98:99], v[98:99], v[82:83], v[106:107]
	v_mfma_f32_32x32x16_bf16 v[2:17], v[26:29], v[2:5], 0
	v_cvt_pk_bf16_f32 v18, v114, v115
	v_mul_f32_e32 v114, v100, v84
	v_mul_f32_e32 v115, v101, v85
	v_fma_f32 v100, v100, v84, v108
	v_fma_f32 v101, v101, v85, v109
	v_pk_add_f32 v[124:125], v[98:99], v[112:113]
	v_pk_add_f32 v[122:123], v[100:101], v[110:111]
	v_cvt_pk_bf16_f32 v101, v108, v109
	v_cvt_pk_bf16_f32 v100, v106, v107
	ds_read_b128 v[106:109], v213 offset:26624
	v_pk_fma_f32 v[116:117], v[32:33], v[20:21], v[24:25]
	v_cvt_pk_bf16_f32 v21, v24, v25
	v_cvt_pk_bf16_f32 v20, v22, v23
	ds_read_b128 v[110:113], v213 offset:27648
	v_cvt_pk_bf16_f32 v99, v114, v115
	v_mfma_f32_32x32x16_bf16 v[18:33], v[26:29], v[18:21], 0
	v_cvt_pk_bf16_f32 v98, v120, v121
	s_waitcnt lgkmcnt(1)
	v_mul_f32_e32 v114, v106, v82
	v_mul_f32_e32 v115, v107, v83
	s_waitcnt lgkmcnt(0)
	v_pk_mul_f32 v[86:87], v[110:111], v[86:87]
	v_pk_mul_f32 v[88:89], v[112:113], v[88:89]
	v_pk_fma_f32 v[82:83], v[106:107], v[82:83], v[86:87]
	v_mfma_f32_32x32x16_bf16 v[2:17], v[102:105], v[98:101], v[2:17]
	v_mul_f32_e32 v98, v108, v84
	v_mul_f32_e32 v99, v109, v85
	v_fma_f32 v84, v108, v84, v88
	v_fma_f32 v85, v109, v85, v89
	v_add_f32_e32 v108, v82, v118
	v_add_f32_e32 v109, v83, v119
	v_cvt_pk_bf16_f32 v83, v98, v99
	v_pk_add_f32 v[106:107], v[84:85], v[116:117]
	v_cvt_pk_bf16_f32 v85, v88, v89
	v_cvt_pk_bf16_f32 v84, v86, v87
	ds_read_b128 v[86:89], v213 offset:38912
	ds_read_b128 v[98:101], v213 offset:20480
	v_cvt_pk_bf16_f32 v82, v114, v115
	s_waitcnt lgkmcnt(0)
	v_pk_mul_f32 v[110:111], v[100:101], v[76:77]
	v_mfma_f32_32x32x16_bf16 v[18:33], v[102:105], v[82:85], v[18:33]
	ds_read_b128 v[82:85], v213 offset:21504
	ds_read_b128 v[102:105], v213 offset:28672
	v_mul_f32_e32 v112, v98, v74
	v_mul_f32_e32 v113, v99, v75
	s_waitcnt lgkmcnt(1)
	v_pk_mul_f32 v[84:85], v[84:85], v[80:81]
	v_pk_mul_f32 v[114:115], v[82:83], v[78:79]
	v_pk_fma_f32 v[82:83], v[100:101], v[76:77], v[84:85]
	v_cvt_pk_bf16_f32 v85, v84, v85
	v_pk_add_f32 v[116:117], v[82:83], v[122:123]
	v_cvt_pk_bf16_f32 v83, v110, v111
	v_cvt_pk_bf16_f32 v84, v114, v115
	v_cvt_pk_bf16_f32 v82, v112, v113
	v_pk_fma_f32 v[98:99], v[98:99], v[74:75], v[114:115]
	s_waitcnt lgkmcnt(0)
	v_pk_mul_f32 v[112:113], v[102:103], v[74:75]
	v_mfma_f32_32x32x16_bf16 v[2:17], v[86:89], v[82:85], v[2:17]
	ds_read_b128 v[82:85], v213 offset:29696
	v_add_f32_e32 v118, v98, v124
	v_add_f32_e32 v119, v99, v125
	v_mul_f32_e32 v110, v104, v76
	v_mul_f32_e32 v111, v105, v77
	ds_read_b128 v[98:101], v213 offset:39936
	s_waitcnt lgkmcnt(1)
	v_pk_mul_f32 v[78:79], v[82:83], v[78:79]
	v_pk_mul_f32 v[80:81], v[84:85], v[80:81]
	v_pk_fma_f32 v[74:75], v[102:103], v[74:75], v[78:79]
	v_pk_fma_f32 v[76:77], v[104:105], v[76:77], v[80:81]
	v_pk_add_f32 v[104:105], v[74:75], v[108:109]
	v_pk_add_f32 v[102:103], v[76:77], v[106:107]
	v_cvt_pk_bf16_f32 v77, v80, v81
	v_cvt_pk_bf16_f32 v76, v78, v79
	ds_read_b128 v[78:81], v213 offset:22528
	ds_read_b128 v[82:85], v213 offset:23552
	v_cvt_pk_bf16_f32 v75, v110, v111
	v_cvt_pk_bf16_f32 v74, v112, v113
	s_waitcnt lgkmcnt(0)
	v_pk_mul_f32 v[82:83], v[82:83], v[70:71]
	v_mfma_f32_32x32x16_bf16 v[18:33], v[86:89], v[74:77], v[18:33]
	v_mul_f32_e32 v74, v80, v68
	v_mul_f32_e32 v75, v81, v69
	v_mul_f32_e32 v76, v84, v72
	v_mul_f32_e32 v77, v85, v73
	v_mul_f32_e32 v86, v78, v66
	v_mul_f32_e32 v87, v79, v67
	v_pk_fma_f32 v[80:81], v[80:81], v[68:69], v[76:77]
	v_pk_fma_f32 v[78:79], v[78:79], v[66:67], v[82:83]
	v_cvt_pk_bf16_f32 v75, v74, v75
	v_pk_add_f32 v[88:89], v[80:81], v[116:117]
	v_pk_add_f32 v[106:107], v[78:79], v[118:119]
	ds_read_b128 v[78:81], v213 offset:30720
	v_cvt_pk_bf16_f32 v77, v76, v77
	v_cvt_pk_bf16_f32 v76, v82, v83
	ds_read_b128 v[82:85], v213 offset:31744
	v_cvt_pk_bf16_f32 v74, v86, v87
	s_waitcnt lgkmcnt(0)
	v_pk_mul_f32 v[72:73], v[84:85], v[72:73]
	v_mfma_f32_32x32x16_bf16 v[2:17], v[98:101], v[74:77], v[2:17]
	v_mul_f32_e32 v74, v80, v68
	v_mul_f32_e32 v75, v81, v69
	v_fma_f32 v68, v80, v68, v72
	v_fma_f32 v69, v81, v69, v73
	v_mul_f32_e32 v70, v82, v70
	v_mul_f32_e32 v71, v83, v71
	v_pk_add_f32 v[84:85], v[68:69], v[102:103]
	v_cvt_pk_bf16_f32 v69, v72, v73
	v_pk_mov_b32 v[72:73], v[96:97], v[94:95] op_sel:[1,0]
	v_mov_b32_e32 v97, v95
	v_pk_add_f32 v[72:73], v[72:73], v[96:97]
	v_pk_mul_f32 v[76:77], v[78:79], v[66:67]
	v_pk_fma_f32 v[66:67], v[78:79], v[66:67], v[70:71]
	v_pk_add_f32 v[72:73], v[72:73], v[72:73] op_sel:[0,1] op_sel_hi:[1,0]
	v_pk_add_f32 v[86:87], v[66:67], v[104:105]
	v_mov_b32_e32 v66, v72
	s_nop 1
	v_permlane32_swap_b32_e32 v72, v66
	v_add_f32_e32 v66, v72, v66
	v_cvt_pk_bf16_f32 v67, v74, v75
	v_rcp_f32_e32 v74, v66
	v_cvt_pk_bf16_f32 v68, v70, v71
	v_cvt_pk_bf16_f32 v66, v76, v77
	v_pk_mul_f32 v[70:71], v[46:47], v[74:75] op_sel_hi:[1,0]
	s_nop 0
	v_mfma_f32_32x32x16_bf16 v[18:33], v[98:101], v[66:69], v[18:33]
	v_mul_f32_e32 v66, v42, v74
	v_mul_f32_e32 v67, v43, v74
	v_pk_mov_b32 v[42:43], v[92:93], v[90:91] op_sel:[1,0]
	v_mov_b32_e32 v93, v91
	v_pk_add_f32 v[42:43], v[42:43], v[92:93]
	v_pk_mul_f32 v[68:69], v[44:45], v[74:75] op_sel_hi:[1,0]
	v_pk_add_f32 v[42:43], v[42:43], v[42:43] op_sel:[0,1] op_sel_hi:[1,0]
	v_pk_mov_b32 v[44:45], v[106:107], v[88:89] op_sel:[1,0]
	v_mov_b32_e32 v43, v42
	s_nop 1
	v_permlane32_swap_b32_e32 v42, v43
	v_add_f32_e32 v42, v42, v43
	v_rcp_f32_e32 v42, v42
	v_mov_b32_e32 v107, v89
	v_pk_add_f32 v[44:45], v[44:45], v[106:107]
	v_pk_mul_f32 v[72:73], v[48:49], v[74:75] op_sel_hi:[1,0]
	v_pk_add_f32 v[44:45], v[44:45], v[44:45] op_sel:[0,1] op_sel_hi:[1,0]
	v_pk_mul_f32 v[36:37], v[36:37], v[74:75] op_sel_hi:[1,0]
	v_pk_mul_f32 v[38:39], v[38:39], v[74:75] op_sel_hi:[1,0]
	v_pk_mul_f32 v[40:41], v[40:41], v[74:75] op_sel_hi:[1,0]
	v_pk_mul_f32 v[34:35], v[34:35], v[74:75] op_sel_hi:[1,0]
	v_pk_mul_f32 v[74:75], v[58:59], v[42:43] op_sel_hi:[1,0]
	v_pk_mul_f32 v[78:79], v[60:61], v[42:43] op_sel_hi:[1,0]
	v_pk_mul_f32 v[80:81], v[62:63], v[42:43] op_sel_hi:[1,0]
	v_pk_mul_f32 v[82:83], v[64:65], v[42:43] op_sel_hi:[1,0]
	v_pk_mul_f32 v[92:93], v[52:53], v[42:43] op_sel_hi:[1,0]
	v_mov_b32_e32 v43, v44
	s_nop 1
	v_permlane32_swap_b32_e32 v44, v43
	v_add_f32_e32 v43, v44, v43
	v_rcp_f32_e32 v76, v43
	v_pk_mul_f32 v[96:97], v[54:55], v[42:43] op_sel_hi:[1,0]
	v_pk_mul_f32 v[94:95], v[56:57], v[42:43] op_sel_hi:[1,0]
	v_pk_mul_f32 v[98:99], v[50:51], v[42:43] op_sel_hi:[1,0]
	v_pk_mul_f32 v[100:101], v[4:5], v[76:77] op_sel_hi:[1,0]
	v_pk_mov_b32 v[4:5], v[86:87], v[84:85] op_sel:[1,0]
	v_mov_b32_e32 v87, v85
	v_pk_add_f32 v[4:5], v[4:5], v[86:87]
	v_pk_mul_f32 v[102:103], v[6:7], v[76:77] op_sel_hi:[1,0]
	v_pk_add_f32 v[104:105], v[4:5], v[4:5] op_sel:[0,1] op_sel_hi:[1,0]
	v_cvt_pk_bf16_f32 v7, v40, v41
	ds_read_b128 v[84:87], v150 offset:52224
	ds_read_b128 v[50:53], v150 offset:35840
	ds_read_b128 v[54:57], v150 offset:36864
	ds_read_b128 v[58:61], v150 offset:37888
	ds_read_b128 v[62:65], v150 offset:38912
	v_cvt_pk_bf16_f32 v6, v38, v39
	v_cvt_pk_bf16_f32 v5, v36, v37
	v_cvt_pk_bf16_f32 v4, v34, v35
	ds_read_b128 v[88:91], v150 offset:53248
	ds_read_b128 v[34:37], v150 offset:39936
	ds_read_b128 v[38:41], v150 offset:40960
	ds_read_b128 v[42:45], v150 offset:41984
	ds_read_b128 v[46:49], v150 offset:43008
	v_cvt_pk_bf16_f32 v95, v94, v95
	v_cvt_pk_bf16_f32 v94, v96, v97
	v_cvt_pk_bf16_f32 v93, v92, v93
	v_cvt_pk_bf16_f32 v92, v98, v99
	s_waitcnt lgkmcnt(5)
	v_mfma_f32_32x32x16_bf16 v[50:65], v[84:87], v[4:7], v[50:65]
	v_mul_f32_e32 v10, v10, v76
	v_mul_f32_e32 v11, v11, v76
	v_mul_f32_e32 v12, v12, v76
	v_mul_f32_e32 v13, v13, v76
	v_mul_f32_e32 v8, v8, v76
	v_mul_f32_e32 v9, v9, v76
	v_mov_b32_e32 v77, v104
	s_nop 1
	v_permlane32_swap_b32_e32 v104, v77
	v_cvt_pk_bf16_f32 v73, v72, v73
	s_waitcnt lgkmcnt(0)
	v_mfma_f32_32x32x16_bf16 v[34:49], v[84:87], v[92:95], v[34:49]
	v_cvt_pk_bf16_f32 v72, v70, v71
	v_cvt_pk_bf16_f32 v70, v66, v67
	v_add_f32_e32 v66, v104, v77
	v_cvt_pk_bf16_f32 v71, v68, v69
	v_rcp_f32_e32 v104, v66
	v_cvt_pk_bf16_f32 v69, v82, v83
	v_cvt_pk_bf16_f32 v68, v80, v81
	v_cvt_pk_bf16_f32 v67, v78, v79
	v_cvt_pk_bf16_f32 v66, v74, v75
	ds_read_b128 v[78:81], v150 offset:54272
	v_mfma_f32_32x32x16_bf16 v[50:65], v[88:91], v[70:73], v[50:65]
	v_mul_f32_e32 v2, v2, v76
	v_mul_f32_e32 v3, v3, v76
	v_mul_f32_e32 v20, v20, v104
	v_mul_f32_e32 v21, v21, v104
	v_cvt_pk_bf16_f32 v85, v8, v9
	v_cvt_pk_bf16_f32 v82, v2, v3
	v_pk_mul_f32 v[2:3], v[22:23], v[104:105] op_sel_hi:[1,0]
	v_pk_mul_f32 v[8:9], v[24:25], v[104:105] op_sel_hi:[1,0]
	v_pk_mul_f32 v[18:19], v[18:19], v[104:105] op_sel_hi:[1,0]
	v_mfma_f32_32x32x16_bf16 v[34:49], v[88:91], v[66:69], v[34:49]
	v_cvt_pk_bf16_f32 v84, v102, v103
	v_cvt_pk_bf16_f32 v83, v100, v101
	ds_read_b128 v[86:89], v150 offset:55296
	v_cvt_pk_bf16_f32 v99, v8, v9
	v_cvt_pk_bf16_f32 v98, v2, v3
	v_cvt_pk_bf16_f32 v97, v20, v21
	v_cvt_pk_bf16_f32 v96, v18, v19
	s_waitcnt lgkmcnt(1)
	v_mfma_f32_32x32x16_bf16 v[50:65], v[78:81], v[82:85], v[50:65]
	v_mul_f32_e32 v2, v14, v76
	v_mul_f32_e32 v3, v15, v76
	v_mul_f32_e32 v8, v16, v76
	v_mul_f32_e32 v9, v17, v76
	v_mul_f32_e32 v14, v26, v104
	v_mul_f32_e32 v15, v27, v104
	v_cvt_pk_bf16_f32 v77, v8, v9
	v_cvt_pk_bf16_f32 v76, v2, v3
	v_cvt_pk_bf16_f32 v74, v10, v11
	v_pk_mul_f32 v[2:3], v[28:29], v[104:105] op_sel_hi:[1,0]
	v_mfma_f32_32x32x16_bf16 v[34:49], v[78:81], v[96:99], v[34:49]
	v_mul_f32_e32 v8, v30, v104
	v_mul_f32_e32 v9, v31, v104
	v_mul_f32_e32 v10, v32, v104
	v_mul_f32_e32 v11, v33, v104
	v_cvt_pk_bf16_f32 v75, v12, v13
	v_cvt_pk_bf16_f32 v81, v10, v11
	v_cvt_pk_bf16_f32 v80, v8, v9
	v_cvt_pk_bf16_f32 v79, v2, v3
	v_cvt_pk_bf16_f32 v78, v14, v15
	s_waitcnt lgkmcnt(0)
	v_mfma_f32_32x32x16_bf16 v[50:65], v[86:89], v[74:77], v[50:65]
	v_mfma_f32_32x32x16_bf16 v[34:49], v[86:89], v[78:81], v[34:49]
	ds_read_b128 v[86:89], v150 offset:56320
	ds_read_b128 v[18:21], v150 offset:44032
	ds_read_b128 v[22:25], v150 offset:45056
	ds_read_b128 v[26:29], v150 offset:46080
	ds_read_b128 v[30:33], v150 offset:47104
	ds_read_b128 v[100:103], v150 offset:57344
	s_waitcnt lgkmcnt(1)
	v_mfma_f32_32x32x16_bf16 v[18:33], v[86:89], v[4:7], v[18:33]
	ds_read_b128 v[2:5], v150 offset:48128
	ds_read_b128 v[6:9], v150 offset:49152
	ds_read_b128 v[10:13], v150 offset:50176
	ds_read_b128 v[14:17], v150 offset:51200
	s_waitcnt lgkmcnt(0)
	v_mfma_f32_32x32x16_bf16 v[2:17], v[86:89], v[92:95], v[2:17]
	v_mfma_f32_32x32x16_bf16 v[18:33], v[100:103], v[70:73], v[18:33]
	v_mfma_f32_32x32x16_bf16 v[2:17], v[100:103], v[66:69], v[2:17]
	ds_read_b128 v[66:69], v150 offset:58368
	ds_read_b128 v[70:73], v150 offset:59392
	s_waitcnt lgkmcnt(1)
	v_mfma_f32_32x32x16_bf16 v[18:33], v[66:69], v[82:85], v[18:33]
	v_mfma_f32_32x32x16_bf16 v[2:17], v[66:69], v[96:99], v[2:17]
	s_waitcnt lgkmcnt(0)
	v_mfma_f32_32x32x16_bf16 v[18:33], v[70:73], v[74:77], v[18:33]
	v_mfma_f32_32x32x16_bf16 v[2:17], v[70:73], v[78:81], v[2:17]
	s_nop 10
	v_mul_f32_e32 v66, v22, v22
	v_mul_f32_e32 v67, v23, v23
	v_mul_f32_e32 v68, v30, v30
	v_mul_f32_e32 v69, v31, v31
	v_mul_f32_e32 v70, v24, v24
	v_mul_f32_e32 v71, v25, v25
	v_pk_mul_f32 v[72:73], v[32:33], v[32:33]
	v_pk_mul_f32 v[74:75], v[20:21], v[20:21]
	v_pk_mul_f32 v[76:77], v[28:29], v[28:29]
	v_pk_mul_f32 v[78:79], v[26:27], v[26:27]
	v_pk_mul_f32 v[80:81], v[18:19], v[18:19]
	v_pk_fma_f32 v[78:79], v[58:59], v[58:59], v[78:79]
	v_pk_fma_f32 v[76:77], v[60:61], v[60:61], v[76:77]
	v_pk_fma_f32 v[74:75], v[52:53], v[52:53], v[74:75]
	v_pk_fma_f32 v[72:73], v[64:65], v[64:65], v[72:73]
	v_pk_fma_f32 v[70:71], v[56:57], v[56:57], v[70:71]
	v_pk_fma_f32 v[68:69], v[62:63], v[62:63], v[68:69]
	v_pk_fma_f32 v[66:67], v[54:55], v[54:55], v[66:67]
	v_pk_fma_f32 v[80:81], v[50:51], v[50:51], v[80:81]
	v_pk_add_f32 v[66:67], v[66:67], v[68:69]
	v_pk_add_f32 v[68:69], v[70:71], v[72:73]
	v_pk_add_f32 v[70:71], v[74:75], v[76:77]
	v_pk_add_f32 v[72:73], v[80:81], v[78:79]
	v_pk_add_f32 v[68:69], v[70:71], v[68:69]
	v_pk_add_f32 v[66:67], v[72:73], v[66:67]
	v_pk_mul_f32 v[72:73], v[14:15], v[14:15]
	v_pk_mov_b32 v[70:71], v[66:67], v[68:69] op_sel:[1,0]
	v_mov_b32_e32 v67, v69
	v_pk_add_f32 v[66:67], v[70:71], v[66:67]
	v_pk_mul_f32 v[70:71], v[6:7], v[6:7]
	v_pk_mul_f32 v[74:75], v[8:9], v[8:9]
	v_pk_mul_f32 v[76:77], v[16:17], v[16:17]
	v_pk_mul_f32 v[78:79], v[4:5], v[4:5]
	v_pk_mul_f32 v[80:81], v[12:13], v[12:13]
	v_pk_mul_f32 v[82:83], v[10:11], v[10:11]
	v_pk_mul_f32 v[84:85], v[2:3], v[2:3]
	v_pk_fma_f32 v[82:83], v[42:43], v[42:43], v[82:83]
	v_pk_fma_f32 v[80:81], v[44:45], v[44:45], v[80:81]
	v_pk_fma_f32 v[78:79], v[36:37], v[36:37], v[78:79]
	v_pk_fma_f32 v[76:77], v[48:49], v[48:49], v[76:77]
	v_pk_fma_f32 v[74:75], v[40:41], v[40:41], v[74:75]
	v_pk_fma_f32 v[72:73], v[46:47], v[46:47], v[72:73]
	v_pk_fma_f32 v[70:71], v[38:39], v[38:39], v[70:71]
	v_pk_fma_f32 v[84:85], v[34:35], v[34:35], v[84:85]
	v_pk_add_f32 v[70:71], v[70:71], v[72:73]
	v_pk_add_f32 v[72:73], v[74:75], v[76:77]
	v_pk_add_f32 v[74:75], v[78:79], v[80:81]
	v_pk_add_f32 v[76:77], v[84:85], v[82:83]
	v_pk_add_f32 v[72:73], v[74:75], v[72:73]
	v_pk_add_f32 v[70:71], v[76:77], v[70:71]
	v_pk_add_f32 v[66:67], v[66:67], v[66:67] op_sel:[0,1] op_sel_hi:[1,0]
	v_pk_mov_b32 v[74:75], v[70:71], v[72:73] op_sel:[1,0]
	v_mov_b32_e32 v71, v73
	v_pk_add_f32 v[70:71], v[74:75], v[70:71]
	v_mov_b32_e32 v69, v66
	v_pk_add_f32 v[70:71], v[70:71], v[70:71] op_sel:[0,1] op_sel_hi:[1,0]
	s_nop 0
	v_permlane32_swap_b32_e32 v66, v69
	v_mov_b32_e32 v68, v70
	s_nop 1
	v_permlane32_swap_b32_e32 v70, v68
	v_mov_b32_e32 v71, v66
	v_pk_add_f32 v[66:67], v[70:71], v[68:69]
	v_pk_fma_f32 v[66:67], v[66:67], s[0:1], v[152:153] op_sel_hi:[1,0,0]
	s_mov_b32 s1, 0x800000
	v_mul_f32_e32 v68, 0x4b800000, v67
	v_cmp_gt_f32_e32 vcc, s1, v67
	s_nop 1
	v_cndmask_b32_e32 v67, v67, v68, vcc
	v_rsq_f32_e32 v67, v67
	s_nop 0
	v_mul_f32_e32 v68, 0x45800000, v67
	v_cndmask_b32_e32 v68, v67, v68, vcc
	v_pk_mul_f32 v[158:159], v[50:51], v[68:69] op_sel_hi:[1,0]
	v_pk_mul_f32 v[50:51], v[18:19], v[68:69] op_sel_hi:[1,0]
	v_mul_f32_e32 v18, 0x4b800000, v66
	v_cmp_gt_f32_e32 vcc, s1, v66
	v_pk_mul_f32 v[80:81], v[60:61], v[68:69] op_sel_hi:[1,0]
	v_pk_mul_f32 v[60:61], v[28:29], v[68:69] op_sel_hi:[1,0]
	v_cndmask_b32_e32 v18, v66, v18, vcc
	v_rsq_f32_e32 v18, v18
	v_pk_mul_f32 v[78:79], v[58:59], v[68:69] op_sel_hi:[1,0]
	v_pk_mul_f32 v[160:161], v[52:53], v[68:69] op_sel_hi:[1,0]
	v_pk_mul_f32 v[82:83], v[54:55], v[68:69] op_sel_hi:[1,0]
	v_mul_f32_e32 v19, 0x45800000, v18
	v_cndmask_b32_e32 v28, v18, v19, vcc
	v_pk_mul_f32 v[168:169], v[56:57], v[68:69] op_sel_hi:[1,0]
	v_pk_mul_f32 v[58:59], v[26:27], v[68:69] op_sel_hi:[1,0]
	v_pk_mul_f32 v[52:53], v[20:21], v[68:69] op_sel_hi:[1,0]
	v_pk_mul_f32 v[54:55], v[22:23], v[68:69] op_sel_hi:[1,0]
	v_pk_mul_f32 v[56:57], v[24:25], v[68:69] op_sel_hi:[1,0]
	v_pk_mul_f32 v[18:19], v[42:43], v[28:29] op_sel_hi:[1,0]
	v_pk_mul_f32 v[20:21], v[44:45], v[28:29] op_sel_hi:[1,0]
	v_pk_mul_f32 v[22:23], v[46:47], v[28:29] op_sel_hi:[1,0]
	v_pk_mul_f32 v[26:27], v[48:49], v[28:29] op_sel_hi:[1,0]
	v_pk_mul_f32 v[162:163], v[34:35], v[28:29] op_sel_hi:[1,0]
	v_pk_mul_f32 v[164:165], v[36:37], v[28:29] op_sel_hi:[1,0]
	v_pk_mul_f32 v[166:167], v[38:39], v[28:29] op_sel_hi:[1,0]
	v_pk_mul_f32 v[24:25], v[40:41], v[28:29] op_sel_hi:[1,0]
	v_pk_mul_f32 v[104:105], v[2:3], v[28:29] op_sel_hi:[1,0]
	v_pk_mul_f32 v[112:113], v[4:5], v[28:29] op_sel_hi:[1,0]
	ds_read_b128 v[2:5], v150 offset:60416
	ds_read_b128 v[34:37], v174 offset:32768
	ds_read_b128 v[38:41], v174 offset:32800
	ds_read_b128 v[42:45], v174 offset:32832
	ds_read_b128 v[46:49], v174 offset:32864
	v_cvt_pk_bf16_f32 v129, v168, v169
	v_cvt_pk_bf16_f32 v128, v82, v83
	v_cvt_pk_bf16_f32 v127, v160, v161
	v_cvt_pk_bf16_f32 v126, v158, v159
	v_cvt_pk_bf16_f32 v137, v24, v25
	v_cvt_pk_bf16_f32 v136, v166, v167
	v_cvt_pk_bf16_f32 v135, v164, v165
	s_waitcnt lgkmcnt(0)
	v_mfma_f32_32x32x16_bf16 v[86:101], v[2:5], v[126:129], v[34:49]
	v_cvt_pk_bf16_f32 v134, v162, v163
	v_mul_f32_e32 v84, v62, v68
	v_mul_f32_e32 v85, v63, v68
	v_mul_f32_e32 v170, v64, v68
	v_mul_f32_e32 v171, v65, v68
	v_pk_mul_f32 v[62:63], v[30:31], v[68:69] op_sel_hi:[1,0]
	v_pk_mul_f32 v[64:65], v[32:33], v[68:69] op_sel_hi:[1,0]
	v_pk_mul_f32 v[116:117], v[6:7], v[28:29] op_sel_hi:[1,0]
	v_pk_mul_f32 v[154:155], v[8:9], v[28:29] op_sel_hi:[1,0]
	v_mfma_f32_32x32x16_bf16 v[34:49], v[2:5], v[134:137], v[34:49]
	ds_read_b128 v[6:9], v150 offset:61440
	ds_read_b128 v[66:69], v174 offset:32896
	ds_read_b128 v[106:109], v150 offset:64512
	v_cvt_pk_bf16_f32 v125, v170, v171
	v_cvt_pk_bf16_f32 v124, v84, v85
	v_cvt_pk_bf16_f32 v123, v80, v81
	v_cvt_pk_bf16_f32 v122, v78, v79
	v_cvt_pk_bf16_f32 v149, v26, v27
	v_cvt_pk_bf16_f32 v148, v22, v23
	v_cvt_pk_bf16_f32 v147, v20, v21
	v_cvt_pk_bf16_f32 v146, v18, v19
	s_waitcnt lgkmcnt(2)
	v_mfma_f32_32x32x16_bf16 v[86:101], v[6:9], v[122:125], v[86:101]
	v_mul_f32_e32 v102, v10, v28
	v_mul_f32_e32 v103, v11, v28
	v_mul_f32_e32 v110, v12, v28
	v_mul_f32_e32 v111, v13, v28
	v_mul_f32_e32 v114, v14, v28
	v_mul_f32_e32 v115, v15, v28
	v_pk_mul_f32 v[156:157], v[16:17], v[28:29] op_sel_hi:[1,0]
	ds_read_b128 v[176:179], v174 offset:33536
	ds_read_b128 v[180:183], v174 offset:33568
	ds_read_b128 v[184:187], v174 offset:33600
	ds_read_b128 v[28:31], v174 offset:33632
	ds_read_b128 v[188:191], v174 offset:33792
	ds_read_b128 v[192:195], v174 offset:33824
	ds_read_b128 v[196:199], v174 offset:33856
	ds_read_b128 v[200:203], v174 offset:33888
	ds_read_b128 v[204:207], v150 offset:62464
	v_cvt_pk_bf16_f32 v133, v56, v57
	v_mfma_f32_32x32x16_bf16 v[34:49], v[6:9], v[146:149], v[34:49]
	v_cvt_pk_bf16_f32 v132, v54, v55
	v_cvt_pk_bf16_f32 v131, v52, v53
	v_cvt_pk_bf16_f32 v130, v50, v51
	ds_read_b128 v[70:73], v174 offset:33664
	ds_read_b128 v[74:77], v174 offset:33920
	ds_read_b128 v[208:211], v150 offset:63488
	v_cvt_pk_bf16_f32 v145, v154, v155
	v_cvt_pk_bf16_f32 v144, v116, v117
	v_cvt_pk_bf16_f32 v143, v112, v113
	v_cvt_pk_bf16_f32 v142, v104, v105
	s_waitcnt lgkmcnt(3)
	v_mfma_f32_32x32x16_bf16 v[86:101], v[204:207], v[130:133], v[86:101]
	v_cvt_pk_bf16_f32 v121, v64, v65
	v_cvt_pk_bf16_f32 v120, v62, v63
	v_cvt_pk_bf16_f32 v119, v60, v61
	v_cvt_pk_bf16_f32 v118, v58, v59
	v_cvt_pk_bf16_f32 v141, v156, v157
	v_cvt_pk_bf16_f32 v140, v114, v115
	v_cvt_pk_bf16_f32 v139, v110, v111
	v_mfma_f32_32x32x16_bf16 v[34:49], v[204:207], v[142:145], v[34:49]
	v_cvt_pk_bf16_f32 v138, v102, v103
	v_fma_f32 v16, v30, v170, v202
	v_fma_f32 v17, v31, v171, v203
	v_fma_f32 v14, v28, v84, v200
	v_fma_f32 v15, v29, v85, v201
	v_pk_fma_f32 v[12:13], v[186:187], v[80:81], v[198:199]
	v_pk_fma_f32 v[10:11], v[184:185], v[78:79], v[196:197]
	v_pk_fma_f32 v[8:9], v[182:183], v[168:169], v[194:195]
	s_waitcnt lgkmcnt(0)
	v_mfma_f32_32x32x16_bf16 v[86:101], v[208:211], v[118:121], v[86:101]
	v_fma_f32 v6, v180, v82, v192
	v_fma_f32 v7, v181, v83, v193
	ds_read_b128 v[78:81], v174 offset:33760
	ds_read_b128 v[82:85], v174 offset:33248
	v_fma_f32 v4, v178, v160, v190
	v_fma_f32 v5, v179, v161, v191
	v_pk_fma_f32 v[2:3], v[176:177], v[158:159], v[188:189]
	v_pk_fma_f32 v[32:33], v[30:31], v[26:27], v[202:203]
	v_pk_fma_f32 v[30:31], v[28:29], v[22:23], v[200:201]
	v_pk_fma_f32 v[28:29], v[186:187], v[20:21], v[198:199]
	v_pk_fma_f32 v[26:27], v[184:185], v[18:19], v[196:197]
	v_pk_fma_f32 v[24:25], v[182:183], v[24:25], v[194:195]
	v_pk_fma_f32 v[22:23], v[180:181], v[166:167], v[192:193]
	v_pk_fma_f32 v[20:21], v[178:179], v[164:165], v[190:191]
	v_pk_fma_f32 v[18:19], v[176:177], v[162:163], v[188:189]
	ds_read_b128 v[158:161], v174 offset:33696
	ds_read_b128 v[162:165], v174 offset:33728
	ds_read_b128 v[166:169], v174 offset:33952
	ds_read_b128 v[176:179], v174 offset:33984
	ds_read_b128 v[180:183], v174 offset:34016
	ds_read_b128 v[184:187], v212 offset:11264
	v_mfma_f32_32x32x16_bf16 v[34:49], v[208:211], v[138:141], v[34:49]
	v_cvt_pk_bf16_f32 v86, v86, v87
	v_cvt_pk_bf16_f32 v87, v88, v89
	v_cvt_pk_bf16_f32 v88, v90, v91
	v_cvt_pk_bf16_f32 v89, v92, v93
	ds_read_b128 v[90:93], v212 offset:12288
	v_pk_max_i16 v86, v86, 0
	v_pk_max_i16 v87, v87, 0
	v_pk_max_i16 v88, v88, 0
	v_pk_max_i16 v89, v89, 0
	s_nop 1
	s_nop 0
	v_cvt_pk_bf16_f32 v188, v34, v35
	v_cvt_pk_bf16_f32 v189, v36, v37
	v_cvt_pk_bf16_f32 v190, v38, v39
	v_cvt_pk_bf16_f32 v191, v40, v41
	s_waitcnt lgkmcnt(1)
	v_mfma_f32_32x32x16_bf16 v[2:17], v[184:187], v[86:89], v[2:17]
	v_pk_max_i16 v188, v188, 0
	v_pk_max_i16 v189, v189, 0
	v_pk_max_i16 v190, v190, 0
	v_pk_max_i16 v191, v191, 0
	v_cvt_pk_bf16_f32 v94, v94, v95
	v_cvt_pk_bf16_f32 v95, v96, v97
	v_cvt_pk_bf16_f32 v96, v98, v99
	v_cvt_pk_bf16_f32 v97, v100, v101
	v_cvt_pk_bf16_f32 v98, v42, v43
	v_cvt_pk_bf16_f32 v99, v44, v45
	v_mfma_f32_32x32x16_bf16 v[18:33], v[184:187], v[188:191], v[18:33]
	ds_read_b128 v[184:187], v212 offset:19456
	v_cvt_pk_bf16_f32 v100, v46, v47
	v_cvt_pk_bf16_f32 v101, v48, v49
	v_fma_f32 v64, v80, v64, v182
	v_fma_f32 v65, v81, v65, v183
	v_pk_fma_f32 v[62:63], v[78:79], v[62:63], v[180:181]
	v_pk_fma_f32 v[60:61], v[164:165], v[60:61], v[178:179]
	v_pk_fma_f32 v[58:59], v[162:163], v[58:59], v[176:177]
	v_pk_max_i16 v94, v94, 0
	v_pk_max_i16 v95, v95, 0
	v_pk_max_i16 v96, v96, 0
	v_pk_max_i16 v97, v97, 0
	v_pk_max_i16 v98, v98, 0
	v_pk_max_i16 v99, v99, 0
	v_pk_max_i16 v100, v100, 0
	v_pk_max_i16 v101, v101, 0
	v_pk_fma_f32 v[56:57], v[160:161], v[56:57], v[168:169]
	s_waitcnt lgkmcnt(1)
	v_mfma_f32_32x32x16_bf16 v[2:17], v[90:93], v[94:97], v[2:17]
	v_fma_f32 v54, v158, v54, v166
	v_fma_f32 v55, v159, v55, v167
	v_fma_f32 v52, v72, v52, v76
	v_fma_f32 v53, v73, v53, v77
	v_fma_f32 v50, v70, v50, v74
	v_fma_f32 v51, v71, v51, v75
	v_pk_fma_f32 v[48:49], v[80:81], v[156:157], v[182:183]
	v_pk_fma_f32 v[46:47], v[78:79], v[114:115], v[180:181]
	v_pk_fma_f32 v[44:45], v[164:165], v[110:111], v[178:179]
	v_pk_fma_f32 v[42:43], v[162:163], v[102:103], v[176:177]
	v_mfma_f32_32x32x16_bf16 v[18:33], v[90:93], v[98:101], v[18:33]
	ds_read_b128 v[90:93], v212 offset:20480
	v_fma_f32 v40, v160, v154, v168
	v_fma_f32 v41, v161, v155, v169
	v_fma_f32 v38, v158, v116, v166
	v_fma_f32 v39, v159, v117, v167
	v_pk_fma_f32 v[36:37], v[72:73], v[112:113], v[76:77]
	v_pk_fma_f32 v[34:35], v[70:71], v[104:105], v[74:75]
	s_waitcnt lgkmcnt(1)
	v_mfma_f32_32x32x16_bf16 v[50:65], v[184:187], v[86:89], v[50:65]
	ds_read_b128 v[70:73], v174 offset:32928
	ds_read_b128 v[74:77], v174 offset:32960
	ds_read_b128 v[78:81], v174 offset:32992
	ds_read_b128 v[86:89], v174 offset:33024
	ds_read_b128 v[110:113], v212 offset:1024
	v_mfma_f32_32x32x16_bf16 v[34:49], v[184:187], v[188:191], v[34:49]
	s_waitcnt lgkmcnt(5)
	v_mfma_f32_32x32x16_bf16 v[50:65], v[90:93], v[94:97], v[50:65]
	v_mfma_f32_32x32x16_bf16 v[34:49], v[90:93], v[98:101], v[34:49]
	s_waitcnt lgkmcnt(2)
	v_mfma_f32_32x32x16_bf16 v[90:105], v[106:109], v[126:129], v[66:81]
	v_mfma_f32_32x32x16_bf16 v[66:81], v[106:109], v[134:137], v[66:81]
	ds_read_b128 v[106:109], v212 offset:0
	s_waitcnt lgkmcnt(0)
	v_mfma_f32_32x32x16_bf16 v[90:105], v[106:109], v[122:125], v[90:105]
	v_mfma_f32_32x32x16_bf16 v[66:81], v[106:109], v[146:149], v[66:81]
	ds_read_b128 v[106:109], v212 offset:2048
	v_mfma_f32_32x32x16_bf16 v[90:105], v[110:113], v[130:133], v[90:105]
	v_mfma_f32_32x32x16_bf16 v[66:81], v[110:113], v[142:145], v[66:81]
	ds_read_b128 v[110:113], v212 offset:13312
	s_waitcnt lgkmcnt(1)
	v_mfma_f32_32x32x16_bf16 v[90:105], v[106:109], v[118:121], v[90:105]
	v_mfma_f32_32x32x16_bf16 v[66:81], v[106:109], v[138:141], v[66:81]
	s_nop 10
	v_cvt_pk_bf16_f32 v90, v90, v91
	v_cvt_pk_bf16_f32 v91, v92, v93
	v_cvt_pk_bf16_f32 v92, v94, v95
	v_cvt_pk_bf16_f32 v94, v98, v99
	v_cvt_pk_bf16_f32 v95, v100, v101
	ds_read_b128 v[98:101], v212 offset:21504
	v_cvt_pk_bf16_f32 v66, v66, v67
	v_cvt_pk_bf16_f32 v67, v68, v69
	v_cvt_pk_bf16_f32 v68, v70, v71
	v_cvt_pk_bf16_f32 v93, v96, v97
	v_cvt_pk_bf16_f32 v69, v72, v73
	ds_read_b128 v[70:73], v212 offset:14336
	v_pk_max_i16 v90, v90, 0
	v_pk_max_i16 v91, v91, 0
	v_pk_max_i16 v92, v92, 0
	v_pk_max_i16 v93, v93, 0
	v_pk_max_i16 v66, v66, 0
	v_pk_max_i16 v67, v67, 0
	v_pk_max_i16 v68, v68, 0
	v_pk_max_i16 v69, v69, 0
	v_cvt_pk_bf16_f32 v96, v102, v103
	s_waitcnt lgkmcnt(2)
	v_mfma_f32_32x32x16_bf16 v[2:17], v[110:113], v[90:93], v[2:17]
	v_cvt_pk_bf16_f32 v97, v104, v105
	v_cvt_pk_bf16_f32 v74, v74, v75
	v_cvt_pk_bf16_f32 v75, v76, v77
	v_cvt_pk_bf16_f32 v76, v78, v79
	v_cvt_pk_bf16_f32 v77, v80, v81
	v_pk_max_i16 v94, v94, 0
	v_pk_max_i16 v95, v95, 0
	v_pk_max_i16 v96, v96, 0
	v_pk_max_i16 v97, v97, 0
	v_pk_max_i16 v74, v74, 0
	v_pk_max_i16 v75, v75, 0
	v_pk_max_i16 v76, v76, 0
	v_pk_max_i16 v77, v77, 0
	v_mfma_f32_32x32x16_bf16 v[18:33], v[110:113], v[66:69], v[18:33]
	s_waitcnt lgkmcnt(1)
	v_mfma_f32_32x32x16_bf16 v[34:49], v[98:101], v[66:69], v[34:49]
	ds_read_b128 v[66:69], v212 offset:22528
	v_mfma_f32_32x32x16_bf16 v[50:65], v[98:101], v[90:93], v[50:65]
	s_waitcnt lgkmcnt(1)
	v_mfma_f32_32x32x16_bf16 v[2:17], v[70:73], v[94:97], v[2:17]
	v_mfma_f32_32x32x16_bf16 v[18:33], v[70:73], v[74:77], v[18:33]
	ds_read_b128 v[78:81], v212 offset:3072
	s_waitcnt lgkmcnt(1)
	v_mfma_f32_32x32x16_bf16 v[50:65], v[66:69], v[94:97], v[50:65]
	ds_read_b128 v[90:93], v174 offset:33056
	ds_read_b128 v[94:97], v174 offset:33088
	ds_read_b128 v[98:101], v174 offset:33120
	ds_read_b128 v[70:73], v174 offset:33152
	v_mfma_f32_32x32x16_bf16 v[34:49], v[66:69], v[74:77], v[34:49]
	ds_read_b128 v[66:69], v212 offset:4096
	ds_read_b128 v[74:77], v212 offset:5120
	s_waitcnt lgkmcnt(3)
	v_mfma_f32_32x32x16_bf16 v[102:117], v[78:81], v[126:129], v[86:101]
	v_mfma_f32_32x32x16_bf16 v[86:101], v[78:81], v[134:137], v[86:101]
	s_waitcnt lgkmcnt(1)
	v_mfma_f32_32x32x16_bf16 v[86:101], v[66:69], v[146:149], v[86:101]
	v_mfma_f32_32x32x16_bf16 v[102:117], v[66:69], v[122:125], v[102:117]
	ds_read_b128 v[66:69], v212 offset:6144
	s_waitcnt lgkmcnt(1)
	v_mfma_f32_32x32x16_bf16 v[86:101], v[74:77], v[142:145], v[86:101]
	v_mfma_f32_32x32x16_bf16 v[102:117], v[74:77], v[130:133], v[102:117]
	ds_read_b128 v[74:77], v212 offset:15360
	s_waitcnt lgkmcnt(1)
	v_mfma_f32_32x32x16_bf16 v[86:101], v[66:69], v[138:141], v[86:101]
	v_mfma_f32_32x32x16_bf16 v[102:117], v[66:69], v[118:121], v[102:117]
	s_nop 10
	v_cvt_pk_bf16_f32 v78, v86, v87
	v_cvt_pk_bf16_f32 v80, v90, v91
	v_cvt_pk_bf16_f32 v79, v88, v89
	v_cvt_pk_bf16_f32 v81, v92, v93
	ds_read_b128 v[86:89], v212 offset:16384
	ds_read_b128 v[90:93], v212 offset:23552
	v_cvt_pk_bf16_f32 v66, v102, v103
	v_cvt_pk_bf16_f32 v67, v104, v105
	v_cvt_pk_bf16_f32 v68, v106, v107
	v_cvt_pk_bf16_f32 v69, v108, v109
	v_pk_max_i16 v66, v66, 0
	v_pk_max_i16 v67, v67, 0
	v_pk_max_i16 v68, v68, 0
	v_pk_max_i16 v69, v69, 0
	v_pk_max_i16 v78, v78, 0
	v_pk_max_i16 v79, v79, 0
	v_pk_max_i16 v80, v80, 0
	v_pk_max_i16 v81, v81, 0
	v_cvt_pk_bf16_f32 v94, v94, v95
	s_waitcnt lgkmcnt(2)
	v_mfma_f32_32x32x16_bf16 v[18:33], v[74:77], v[78:81], v[18:33]
	v_cvt_pk_bf16_f32 v95, v96, v97
	v_cvt_pk_bf16_f32 v96, v98, v99
	v_cvt_pk_bf16_f32 v97, v100, v101
	v_pk_max_i16 v94, v94, 0
	v_pk_max_i16 v95, v95, 0
	v_pk_max_i16 v96, v96, 0
	v_pk_max_i16 v97, v97, 0
	v_mfma_f32_32x32x16_bf16 v[2:17], v[74:77], v[66:69], v[2:17]
	v_cvt_pk_bf16_f32 v74, v110, v111
	v_cvt_pk_bf16_f32 v75, v112, v113
	v_cvt_pk_bf16_f32 v76, v114, v115
	v_cvt_pk_bf16_f32 v77, v116, v117
	v_pk_max_i16 v74, v74, 0
	v_pk_max_i16 v75, v75, 0
	v_pk_max_i16 v76, v76, 0
	v_pk_max_i16 v77, v77, 0
	s_waitcnt lgkmcnt(0)
	v_mfma_f32_32x32x16_bf16 v[50:65], v[90:93], v[66:69], v[50:65]
	ds_read_b128 v[66:69], v212 offset:24576
	v_mfma_f32_32x32x16_bf16 v[34:49], v[90:93], v[78:81], v[34:49]
	ds_read_b128 v[102:105], v212 offset:7168
	v_mfma_f32_32x32x16_bf16 v[2:17], v[86:89], v[74:77], v[2:17]
	s_waitcnt lgkmcnt(1)
	v_mfma_f32_32x32x16_bf16 v[50:65], v[66:69], v[74:77], v[50:65]
	ds_read_b128 v[74:77], v174 offset:33184
	ds_read_b128 v[78:81], v174 offset:33216
	v_mfma_f32_32x32x16_bf16 v[34:49], v[66:69], v[94:97], v[34:49]
	ds_read_b128 v[66:69], v212 offset:8192
	v_mfma_f32_32x32x16_bf16 v[18:33], v[86:89], v[94:97], v[18:33]
	s_waitcnt lgkmcnt(1)
	v_mfma_f32_32x32x16_bf16 v[86:101], v[102:105], v[126:129], v[70:85]
	v_mfma_f32_32x32x16_bf16 v[70:85], v[102:105], v[134:137], v[70:85]
	ds_read_b128 v[102:105], v212 offset:9216
	v_lshlrev_b32_e32 v135, 2, v1
	v_add_u32_e32 v134, v172, v174
	s_waitcnt lgkmcnt(1)
	v_mfma_f32_32x32x16_bf16 v[86:101], v[66:69], v[122:125], v[86:101]
	v_mfma_f32_32x32x16_bf16 v[70:85], v[66:69], v[146:149], v[70:85]
	ds_read_b128 v[66:69], v212 offset:10240
	s_waitcnt lgkmcnt(1)
	v_mfma_f32_32x32x16_bf16 v[86:101], v[102:105], v[130:133], v[86:101]
	v_mfma_f32_32x32x16_bf16 v[70:85], v[102:105], v[142:145], v[70:85]
	ds_read_b128 v[102:105], v212 offset:17408
	s_waitcnt lgkmcnt(1)
	v_mfma_f32_32x32x16_bf16 v[86:101], v[66:69], v[118:121], v[86:101]
	v_mfma_f32_32x32x16_bf16 v[70:85], v[66:69], v[138:141], v[70:85]
	s_nop 10
	v_cvt_pk_bf16_f32 v68, v90, v91
	v_cvt_pk_bf16_f32 v69, v92, v93
	ds_read_b128 v[90:93], v212 offset:25600
	v_cvt_pk_bf16_f32 v66, v86, v87
	v_cvt_pk_bf16_f32 v67, v88, v89
	v_pk_max_i16 v66, v66, 0
	v_pk_max_i16 v67, v67, 0
	v_pk_max_i16 v68, v68, 0
	v_pk_max_i16 v69, v69, 0
	v_cvt_pk_bf16_f32 v70, v70, v71
	v_cvt_pk_bf16_f32 v71, v72, v73
	s_waitcnt lgkmcnt(1)
	v_mfma_f32_32x32x16_bf16 v[2:17], v[102:105], v[66:69], v[2:17]
	v_cvt_pk_bf16_f32 v72, v74, v75
	v_cvt_pk_bf16_f32 v73, v76, v77
	ds_read_b128 v[74:77], v212 offset:18432
	v_cvt_pk_bf16_f32 v86, v94, v95
	v_cvt_pk_bf16_f32 v87, v96, v97
	v_cvt_pk_bf16_f32 v88, v98, v99
	s_waitcnt lgkmcnt(1)
	v_mfma_f32_32x32x16_bf16 v[50:65], v[90:93], v[66:69], v[50:65]
	ds_read_b128 v[66:69], v212 offset:26624
	v_cvt_pk_bf16_f32 v89, v100, v101
	v_pk_max_i16 v86, v86, 0
	v_pk_max_i16 v87, v87, 0
	v_pk_max_i16 v88, v88, 0
	v_pk_max_i16 v89, v89, 0
	v_pk_max_i16 v70, v70, 0
	v_pk_max_i16 v71, v71, 0
	v_pk_max_i16 v72, v72, 0
	v_pk_max_i16 v73, v73, 0
	v_cvt_pk_bf16_f32 v78, v78, v79
	v_cvt_pk_bf16_f32 v79, v80, v81
	s_waitcnt lgkmcnt(1)
	v_mfma_f32_32x32x16_bf16 v[2:17], v[74:77], v[86:89], v[2:17]
	v_cvt_pk_bf16_f32 v80, v82, v83
	v_cvt_pk_bf16_f32 v81, v84, v85
	v_pk_max_i16 v78, v78, 0
	v_pk_max_i16 v79, v79, 0
	v_pk_max_i16 v80, v80, 0
	v_pk_max_i16 v81, v81, 0
	s_waitcnt lgkmcnt(0)
	v_mfma_f32_32x32x16_bf16 v[50:65], v[66:69], v[86:89], v[50:65]
	v_mfma_f32_32x32x16_bf16 v[34:49], v[90:93], v[70:73], v[34:49]
	s_nop 10
	v_add_f32_e32 v130, v10, v58
	v_add_f32_e32 v131, v11, v59
	v_add_f32_e32 v132, v12, v60
	v_add_f32_e32 v133, v13, v61
	v_add_f32_e32 v138, v4, v52
	v_add_f32_e32 v139, v5, v53
	v_pk_add_f32 v[140:141], v[16:17], v[64:65]
	v_pk_add_f32 v[142:143], v[8:9], v[56:57]
	v_pk_add_f32 v[144:145], v[14:15], v[62:63]
	v_pk_add_f32 v[146:147], v[6:7], v[54:55]
	v_mfma_f32_32x32x16_bf16 v[18:33], v[102:105], v[70:73], v[18:33]
	ds_read2st64_b32 v[70:71], v135 offset0:133 offset1:134
	v_add_f32_e32 v148, v2, v50
	v_add_f32_e32 v149, v3, v51
	v_add_f32_e32 v144, v146, v144
	v_add_f32_e32 v145, v147, v145
	v_pk_add_f32 v[140:141], v[142:143], v[140:141]
	v_pk_add_f32 v[132:133], v[138:139], v[132:133]
	v_pk_add_f32 v[130:131], v[148:149], v[130:131]
	v_pk_add_f32 v[132:133], v[132:133], v[140:141]
	v_pk_add_f32 v[130:131], v[130:131], v[144:145]
	v_mfma_f32_32x32x16_bf16 v[34:49], v[66:69], v[78:81], v[34:49]
	v_pk_mov_b32 v[138:139], v[130:131], v[132:133] op_sel:[1,0]
	v_mov_b32_e32 v131, v133
	s_waitcnt vmcnt(0) lgkmcnt(0)
	v_mul_f32_e32 v66, v175, v70
	v_pk_add_f32 v[130:131], v[138:139], v[130:131]
	ds_write_b32 v173, v66 offset:512
	v_mul_f32_e32 v66, v175, v71
	v_pk_add_f32 v[130:131], v[130:131], v[130:131] op_sel:[0,1] op_sel_hi:[1,0]
	s_waitcnt lgkmcnt(0)
	ds_read_b128 v[102:105], v174 offset:34560
	ds_read_b128 v[98:101], v174 offset:34592
	ds_read_b128 v[110:113], v174 offset:34624
	ds_read_b128 v[106:109], v174 offset:34656
	ds_read_b128 v[114:117], v174 offset:34688
	ds_read_b128 v[122:125], v174 offset:34720
	ds_read_b128 v[118:121], v174 offset:34752
	ds_read_b128 v[126:129], v174 offset:34784
	v_mov_b32_dpp v66, v66 quad_perm:[1,0,3,2] row_mask:0xf bank_mask:0xf bound_ctrl:1
	v_mov_b32_e32 v131, v130
	v_fmac_f32_e32 v66, v175, v71
	s_nop 0
	v_permlane32_swap_b32_e32 v130, v131
	v_add_f32_dpp v66, v66, v66 quad_perm:[2,3,0,1] row_mask:0xf bank_mask:0xf bound_ctrl:1
	v_add_f32_e32 v130, v130, v131
	v_fmamk_f32 v65, v130, 0xbc800000, v65
	v_add_f32_dpp v66, v66, v66 row_half_mirror row_mask:0xf bank_mask:0xf bound_ctrl:1
	v_fmamk_f32 v64, v130, 0xbc800000, v64
	v_fmamk_f32 v63, v130, 0xbc800000, v63
	v_fmamk_f32 v62, v130, 0xbc800000, v62
	v_fmamk_f32 v61, v130, 0xbc800000, v61
	v_fmamk_f32 v60, v130, 0xbc800000, v60
	v_fmamk_f32 v59, v130, 0xbc800000, v59
	v_fmamk_f32 v58, v130, 0xbc800000, v58
	v_fmamk_f32 v57, v130, 0xbc800000, v57
	v_fmamk_f32 v56, v130, 0xbc800000, v56
	v_fmamk_f32 v55, v130, 0xbc800000, v55
	v_fmamk_f32 v54, v130, 0xbc800000, v54
	v_fmamk_f32 v53, v130, 0xbc800000, v53
	v_fmamk_f32 v52, v130, 0xbc800000, v52
	v_fmamk_f32 v51, v130, 0xbc800000, v51
	v_fmac_f32_e32 v50, 0xbc800000, v130
	v_add_f32_dpp v66, v66, v66 row_ror:8 row_mask:0xf bank_mask:0xf bound_ctrl:1
	v_fmamk_f32 v17, v130, 0xbc800000, v17
	v_fmamk_f32 v16, v130, 0xbc800000, v16
	v_fmamk_f32 v15, v130, 0xbc800000, v15
	v_fmamk_f32 v14, v130, 0xbc800000, v14
	v_fmamk_f32 v13, v130, 0xbc800000, v13
	v_fmamk_f32 v12, v130, 0xbc800000, v12
	v_fmamk_f32 v11, v130, 0xbc800000, v11
	v_fmamk_f32 v10, v130, 0xbc800000, v10
	v_fmamk_f32 v9, v130, 0xbc800000, v9
	v_fmamk_f32 v8, v130, 0xbc800000, v8
	v_fmamk_f32 v7, v130, 0xbc800000, v7
	v_fmamk_f32 v6, v130, 0xbc800000, v6
	v_fmamk_f32 v5, v130, 0xbc800000, v5
	v_fmamk_f32 v4, v130, 0xbc800000, v4
	v_fmamk_f32 v3, v130, 0xbc800000, v3
	v_fmac_f32_e32 v2, 0xbc800000, v130
	v_pk_mul_f32 v[130:131], v[54:55], v[54:55]
	v_pk_mul_f32 v[132:133], v[62:63], v[62:63]
	v_pk_mul_f32 v[138:139], v[50:51], v[50:51]
	v_pk_mul_f32 v[140:141], v[58:59], v[58:59]
	v_pk_mul_f32 v[142:143], v[56:57], v[56:57]
	v_pk_mul_f32 v[144:145], v[64:65], v[64:65]
	v_pk_mul_f32 v[146:147], v[52:53], v[52:53]
	v_pk_mul_f32 v[148:149], v[60:61], v[60:61]
	v_mov_b32_e32 v67, v66
	v_pk_fma_f32 v[148:149], v[12:13], v[12:13], v[148:149]
	v_pk_fma_f32 v[146:147], v[4:5], v[4:5], v[146:147]
	v_pk_fma_f32 v[144:145], v[16:17], v[16:17], v[144:145]
	v_pk_fma_f32 v[142:143], v[8:9], v[8:9], v[142:143]
	v_pk_fma_f32 v[140:141], v[10:11], v[10:11], v[140:141]
	v_pk_fma_f32 v[138:139], v[2:3], v[2:3], v[138:139]
	v_pk_fma_f32 v[132:133], v[14:15], v[14:15], v[132:133]
	v_pk_fma_f32 v[130:131], v[6:7], v[6:7], v[130:131]
	v_permlane16_swap_b32_e32 v66, v67
	v_pk_add_f32 v[130:131], v[130:131], v[132:133]
	v_pk_add_f32 v[132:133], v[138:139], v[140:141]
	v_pk_add_f32 v[138:139], v[142:143], v[144:145]
	v_pk_add_f32 v[140:141], v[146:147], v[148:149]
	v_mfma_f32_32x32x16_bf16 v[18:33], v[74:77], v[78:81], v[18:33]
	v_add_f32_e32 v136, v66, v67
	ds_read_b128 v[70:73], v134 offset:512
	ds_read_b128 v[66:69], v134 offset:544
	ds_read_b128 v[78:81], v134 offset:576
	ds_read_b128 v[74:77], v134 offset:608
	ds_read_b128 v[82:85], v134 offset:640
	ds_read_b128 v[90:93], v134 offset:672
	ds_read_b128 v[86:89], v134 offset:704
	ds_read_b128 v[94:97], v134 offset:736
	v_pk_add_f32 v[138:139], v[140:141], v[138:139]
	v_pk_add_f32 v[130:131], v[132:133], v[130:131]
	s_waitcnt lgkmcnt(8)
	v_pk_mul_f32 v[140:141], v[126:127], v[62:63]
	v_pk_mov_b32 v[132:133], v[130:131], v[138:139] op_sel:[1,0]
	v_mov_b32_e32 v131, v139
	v_pk_mul_f32 v[138:139], v[122:123], v[54:55]
	v_pk_mul_f32 v[142:143], v[114:115], v[50:51]
	v_pk_mul_f32 v[144:145], v[118:119], v[58:59]
	v_pk_mul_f32 v[146:147], v[124:125], v[56:57]
	v_pk_mul_f32 v[148:149], v[128:129], v[64:65]
	v_pk_mul_f32 v[154:155], v[116:117], v[52:53]
	v_pk_mul_f32 v[156:157], v[120:121], v[60:61]
	v_pk_fma_f32 v[154:155], v[104:105], v[4:5], v[154:155]
	v_pk_fma_f32 v[156:157], v[112:113], v[12:13], v[156:157]
	v_pk_fma_f32 v[148:149], v[108:109], v[16:17], v[148:149]
	v_pk_fma_f32 v[146:147], v[100:101], v[8:9], v[146:147]
	v_pk_fma_f32 v[144:145], v[110:111], v[10:11], v[144:145]
	v_pk_fma_f32 v[142:143], v[102:103], v[2:3], v[142:143]
	v_pk_fma_f32 v[140:141], v[106:107], v[14:15], v[140:141]
	v_pk_fma_f32 v[138:139], v[98:99], v[6:7], v[138:139]
	v_pk_add_f32 v[130:131], v[132:133], v[130:131]
	v_pk_add_f32 v[138:139], v[138:139], v[140:141]
	v_pk_add_f32 v[140:141], v[142:143], v[144:145]
	v_pk_add_f32 v[142:143], v[146:147], v[148:149]
	v_pk_add_f32 v[144:145], v[154:155], v[156:157]
	v_pk_add_f32 v[132:133], v[130:131], v[130:131] op_sel:[0,1] op_sel_hi:[1,0]
	v_pk_add_f32 v[142:143], v[144:145], v[142:143]
	v_pk_add_f32 v[138:139], v[140:141], v[138:139]
	v_add_f32_e32 v133, v142, v143
	v_add_f32_e32 v130, v138, v139
	s_waitcnt lgkmcnt(2)
	v_pk_mul_f32 v[138:139], v[90:91], v[54:55]
	s_waitcnt lgkmcnt(0)
	v_pk_mul_f32 v[140:141], v[94:95], v[62:63]
	v_pk_mul_f32 v[142:143], v[82:83], v[50:51]
	v_pk_mul_f32 v[144:145], v[86:87], v[58:59]
	v_pk_mul_f32 v[146:147], v[92:93], v[56:57]
	v_pk_mul_f32 v[148:149], v[96:97], v[64:65]
	v_pk_mul_f32 v[154:155], v[84:85], v[52:53]
	v_pk_mul_f32 v[156:157], v[88:89], v[60:61]
	v_add_f32_e32 v130, v130, v133
	v_pk_fma_f32 v[156:157], v[80:81], v[12:13], v[156:157]
	v_pk_fma_f32 v[154:155], v[72:73], v[4:5], v[154:155]
	v_pk_fma_f32 v[148:149], v[76:77], v[16:17], v[148:149]
	v_pk_fma_f32 v[146:147], v[68:69], v[8:9], v[146:147]
	v_pk_fma_f32 v[144:145], v[78:79], v[10:11], v[144:145]
	v_pk_fma_f32 v[142:143], v[70:71], v[2:3], v[142:143]
	v_pk_fma_f32 v[140:141], v[74:75], v[14:15], v[140:141]
	v_pk_fma_f32 v[138:139], v[66:67], v[6:7], v[138:139]
	v_mov_b32_e32 v133, v130
	v_pk_add_f32 v[138:139], v[138:139], v[140:141]
	v_pk_add_f32 v[140:141], v[142:143], v[144:145]
	v_pk_add_f32 v[142:143], v[146:147], v[148:149]
	v_pk_add_f32 v[144:145], v[154:155], v[156:157]
	v_permlane32_swap_b32_e32 v130, v133
	v_pk_add_f32 v[142:143], v[144:145], v[142:143]
	v_add_f32_e32 v160, v130, v133
	v_pk_add_f32 v[138:139], v[140:141], v[138:139]
	v_add_f32_e32 v133, v142, v143
	v_pk_add_f32 v[140:141], v[26:27], v[42:43]
	v_pk_add_f32 v[142:143], v[28:29], v[44:45]
	v_pk_add_f32 v[144:145], v[20:21], v[36:37]
	v_pk_add_f32 v[146:147], v[32:33], v[48:49]
	v_pk_add_f32 v[148:149], v[24:25], v[40:41]
	v_pk_add_f32 v[154:155], v[30:31], v[46:47]
	v_pk_add_f32 v[156:157], v[22:23], v[38:39]
	v_pk_add_f32 v[158:159], v[18:19], v[34:35]
	v_pk_add_f32 v[154:155], v[156:157], v[154:155]
	v_pk_add_f32 v[146:147], v[148:149], v[146:147]
	v_pk_add_f32 v[142:143], v[144:145], v[142:143]
	v_pk_add_f32 v[140:141], v[158:159], v[140:141]
	v_pk_add_f32 v[142:143], v[142:143], v[146:147]
	v_pk_add_f32 v[140:141], v[140:141], v[154:155]
	v_add_f32_e32 v130, v138, v139
	v_pk_mov_b32 v[144:145], v[140:141], v[142:143] op_sel:[1,0]
	v_mov_b32_e32 v141, v143
	v_pk_add_f32 v[140:141], v[144:145], v[140:141]
	v_add_f32_e32 v133, v130, v133
	v_pk_add_f32 v[140:141], v[140:141], v[140:141] op_sel:[0,1] op_sel_hi:[1,0]
	v_mov_b32_e32 v131, v132
	v_mov_b32_e32 v130, v140
	s_nop 1
	v_permlane32_swap_b32_e32 v140, v130
	v_add_f32_e32 v130, v140, v130
	v_fmamk_f32 v49, v130, 0xbc800000, v49
	v_fmamk_f32 v48, v130, 0xbc800000, v48
	v_fmamk_f32 v47, v130, 0xbc800000, v47
	v_fmamk_f32 v46, v130, 0xbc800000, v46
	v_fmamk_f32 v45, v130, 0xbc800000, v45
	v_fmamk_f32 v44, v130, 0xbc800000, v44
	v_fmamk_f32 v43, v130, 0xbc800000, v43
	v_fmamk_f32 v42, v130, 0xbc800000, v42
	v_fmamk_f32 v41, v130, 0xbc800000, v41
	v_fmamk_f32 v40, v130, 0xbc800000, v40
	v_fmamk_f32 v39, v130, 0xbc800000, v39
	v_fmamk_f32 v38, v130, 0xbc800000, v38
	v_fmamk_f32 v37, v130, 0xbc800000, v37
	v_fmamk_f32 v36, v130, 0xbc800000, v36
	v_fmamk_f32 v35, v130, 0xbc800000, v35
	v_fmac_f32_e32 v34, 0xbc800000, v130
	v_fmamk_f32 v33, v130, 0xbc800000, v33
	v_fmamk_f32 v32, v130, 0xbc800000, v32
	v_fmamk_f32 v31, v130, 0xbc800000, v31
	v_fmamk_f32 v30, v130, 0xbc800000, v30
	v_fmamk_f32 v29, v130, 0xbc800000, v29
	v_fmamk_f32 v28, v130, 0xbc800000, v28
	v_fmamk_f32 v27, v130, 0xbc800000, v27
	v_fmamk_f32 v26, v130, 0xbc800000, v26
	v_fmamk_f32 v25, v130, 0xbc800000, v25
	v_fmamk_f32 v24, v130, 0xbc800000, v24
	v_fmamk_f32 v23, v130, 0xbc800000, v23
	v_fmamk_f32 v22, v130, 0xbc800000, v22
	v_fmamk_f32 v21, v130, 0xbc800000, v21
	v_fmamk_f32 v20, v130, 0xbc800000, v20
	v_fmamk_f32 v19, v130, 0xbc800000, v19
	v_fmac_f32_e32 v18, 0xbc800000, v130
	v_pk_mul_f32 v[140:141], v[38:39], v[38:39]
	v_pk_mul_f32 v[142:143], v[46:47], v[46:47]
	v_pk_mul_f32 v[144:145], v[34:35], v[34:35]
	v_pk_mul_f32 v[146:147], v[42:43], v[42:43]
	v_pk_mul_f32 v[148:149], v[40:41], v[40:41]
	v_pk_mul_f32 v[154:155], v[48:49], v[48:49]
	v_pk_mul_f32 v[156:157], v[36:37], v[36:37]
	v_pk_mul_f32 v[158:159], v[44:45], v[44:45]
	v_pk_fma_f32 v[156:157], v[20:21], v[20:21], v[156:157]
	v_pk_fma_f32 v[158:159], v[28:29], v[28:29], v[158:159]
	v_pk_fma_f32 v[154:155], v[32:33], v[32:33], v[154:155]
	v_pk_fma_f32 v[148:149], v[24:25], v[24:25], v[148:149]
	v_pk_fma_f32 v[146:147], v[26:27], v[26:27], v[146:147]
	v_pk_fma_f32 v[144:145], v[18:19], v[18:19], v[144:145]
	v_pk_fma_f32 v[142:143], v[30:31], v[30:31], v[142:143]
	v_pk_fma_f32 v[140:141], v[22:23], v[22:23], v[140:141]
	v_permlane32_swap_b32_e32 v132, v131
	v_pk_add_f32 v[140:141], v[140:141], v[142:143]
	v_pk_add_f32 v[142:143], v[144:145], v[146:147]
	v_pk_add_f32 v[144:145], v[148:149], v[154:155]
	v_pk_add_f32 v[146:147], v[156:157], v[158:159]
	v_pk_add_f32 v[140:141], v[142:143], v[140:141]
	v_pk_add_f32 v[144:145], v[146:147], v[144:145]
	v_pk_mul_f32 v[122:123], v[122:123], v[38:39]
	v_pk_mov_b32 v[142:143], v[140:141], v[144:145] op_sel:[1,0]
	v_mov_b32_e32 v141, v145
	v_pk_add_f32 v[140:141], v[142:143], v[140:141]
	v_pk_mul_f32 v[126:127], v[126:127], v[46:47]
	v_pk_add_f32 v[140:141], v[140:141], v[140:141] op_sel:[0,1] op_sel_hi:[1,0]
	v_pk_mul_f32 v[114:115], v[114:115], v[34:35]
	v_mov_b32_e32 v130, v140
	s_nop 1
	v_permlane32_swap_b32_e32 v140, v130
	v_mov_b32_e32 v141, v132
	v_pk_add_f32 v[130:131], v[140:141], v[130:131]
	v_pk_mul_f32 v[118:119], v[118:119], v[42:43]
	v_pk_fma_f32 v[130:131], v[130:131], s[0:1], v[152:153] op_sel_hi:[1,0,0]
	v_pk_mul_f32 v[124:125], v[124:125], v[40:41]
	v_mul_f32_e32 v132, 0x4b800000, v131
	v_cmp_gt_f32_e32 vcc, s1, v131
	v_pk_mul_f32 v[128:129], v[128:129], v[48:49]
	v_pk_mul_f32 v[116:117], v[116:117], v[36:37]
	v_pk_mul_f32 v[120:121], v[120:121], v[44:45]
	v_cndmask_b32_e32 v131, v131, v132, vcc
	v_mul_f32_e32 v132, 0x4b800000, v130
	v_cmp_gt_f32_e64 s[0:1], s1, v130
	v_pk_fma_f32 v[112:113], v[112:113], v[28:29], v[120:121]
	v_pk_fma_f32 v[104:105], v[104:105], v[20:21], v[116:117]
	v_pk_fma_f32 v[108:109], v[108:109], v[32:33], v[128:129]
	v_pk_fma_f32 v[100:101], v[100:101], v[24:25], v[124:125]
	v_pk_fma_f32 v[110:111], v[110:111], v[26:27], v[118:119]
	v_pk_fma_f32 v[102:103], v[102:103], v[18:19], v[114:115]
	v_pk_fma_f32 v[106:107], v[106:107], v[30:31], v[126:127]
	v_pk_fma_f32 v[98:99], v[98:99], v[22:23], v[122:123]
	v_rsq_f32_e32 v131, v131
	v_cndmask_b32_e64 v130, v130, v132, s[0:1]
	v_pk_add_f32 v[98:99], v[98:99], v[106:107]
	v_pk_add_f32 v[102:103], v[102:103], v[110:111]
	v_pk_add_f32 v[100:101], v[100:101], v[108:109]
	v_pk_add_f32 v[104:105], v[104:105], v[112:113]
	v_rsq_f32_e32 v132, v130
	v_pk_add_f32 v[100:101], v[104:105], v[100:101]
	v_pk_add_f32 v[98:99], v[102:103], v[98:99]
	v_mul_f32_e32 v130, 0x45800000, v131
	v_add_f32_e32 v98, v98, v99
	v_add_f32_e32 v99, v100, v101
	v_add_f32_e32 v98, v98, v99
	v_mov_b32_e32 v99, v98
	v_pk_mul_f32 v[90:91], v[90:91], v[38:39]
	v_pk_mul_f32 v[94:95], v[94:95], v[46:47]
	v_pk_mul_f32 v[82:83], v[82:83], v[34:35]
	v_pk_mul_f32 v[86:87], v[86:87], v[42:43]
	v_cndmask_b32_e32 v130, v131, v130, vcc
	v_mul_f32_e32 v131, 0x45800000, v132
	v_permlane32_swap_b32_e32 v98, v99
	v_pk_fma_f32 v[78:79], v[78:79], v[26:27], v[86:87]
	v_pk_fma_f32 v[70:71], v[70:71], v[18:19], v[82:83]
	v_pk_fma_f32 v[74:75], v[74:75], v[30:31], v[94:95]
	v_pk_fma_f32 v[66:67], v[66:67], v[22:23], v[90:91]
	v_cndmask_b32_e64 v131, v132, v131, s[0:1]
	v_add_f32_e32 v98, v98, v99
	v_pk_add_f32 v[66:67], v[66:67], v[74:75]
	v_pk_add_f32 v[70:71], v[70:71], v[78:79]
	v_mul_f32_e32 v139, v160, v130
	v_mul_f32_e32 v98, v98, v131
	v_pk_add_f32 v[66:67], v[70:71], v[66:67]
	v_cmp_gt_u32_e32 vcc, 32, v1
	v_add_f32_e32 v66, v66, v67
	v_pk_mul_f32 v[92:93], v[92:93], v[40:41]
	v_cndmask_b32_e32 v67, v98, v139, vcc
	v_add_f32_e32 v67, s12, v67
	v_pk_mul_f32 v[96:97], v[96:97], v[48:49]
	v_pk_mul_f32 v[84:85], v[84:85], v[36:37]
	v_pk_mul_f32 v[88:89], v[88:89], v[44:45]
	v_mul_f32_e32 v67, 0xbfb8aa3b, v67
	v_pk_fma_f32 v[80:81], v[80:81], v[28:29], v[88:89]
	v_pk_fma_f32 v[72:73], v[72:73], v[20:21], v[84:85]
	v_pk_fma_f32 v[76:77], v[76:77], v[32:33], v[96:97]
	v_pk_fma_f32 v[68:69], v[68:69], v[24:25], v[92:93]
	v_exp_f32_e32 v70, v67
	v_pk_add_f32 v[68:69], v[68:69], v[76:77]
	v_pk_add_f32 v[72:73], v[72:73], v[80:81]
	v_cmp_lt_i32_e64 s[0:1], 0, v151
	v_pk_add_f32 v[68:69], v[72:73], v[68:69]
	v_mov_b32_e32 v137, v136
	v_add_f32_e32 v67, v68, v69
	v_add_f32_e32 v67, v66, v67
	v_add_f32_e32 v66, 1.0, v70
	v_rcp_f32_e32 v66, v66
	v_mov_b32_e32 v69, 0xff800000
	v_mov_b32_e32 v138, v133
	v_mov_b32_e32 v68, v67
	v_cndmask_b32_e64 v70, v69, v66, s[0:1]
	v_mbcnt_lo_u32_b32 v66, -1, 0
	v_mbcnt_hi_u32_b32 v66, -1, v66
	v_permlane32_swap_b32_e32 v136, v137
	v_permlane32_swap_b32_e32 v133, v138
	v_permlane32_swap_b32_e32 v67, v68
	v_and_b32_e32 v86, 64, v66
	s_mov_b32 s14, 8
	s_mov_b32 s13, 0
	v_mov_b32_e32 v66, 0
	s_waitcnt lgkmcnt(0)
